# weight-copy partition: 1024 more MoE items per layer moved from the prologue to the forgetting-attention workgroups' slack at the end of the attention phase
# speedup vs baseline: 1.0021x; 1.0021x over previous
.LBB0_16:
	s_mul_i32 s0, s33, 0x4200
	s_add_i32 s0, s0, 0
	v_writelane_b32 v247, s22, 11
	s_cmpk_lg_i32 s3, 0x100
	v_writelane_b32 v247, s0, 13
	s_cselect_b64 s[0:1], -1, 0
	s_cmpk_eq_i32 s3, 0x100
	v_writelane_b32 v247, s0, 14
	s_cselect_b64 s[36:37], -1, 0
	s_mov_b32 s5, 0
	v_writelane_b32 v247, s1, 15
	s_and_b64 s[0:1], s[36:37], exec
	s_cselect_b32 s0, 0x1800, 0
	s_sub_i32 s1, 0x6000, s0
	s_lshl_b32 s14, s1, 1
	s_addk_i32 s14, 0x1700
	s_cmp_ge_i32 s56, s14
	s_movk_i32 s15, 0x6000
	s_waitcnt lgkmcnt(0)
	s_barrier
	s_cbranch_scc1 .LBB0_27
	v_lshlrev_b32_e32 v0, 1, v12
	v_ashrrev_i32_e32 v4, 5, v12
	v_and_b32_e32 v0, 62, v0
	s_movk_i32 s4, 0x104
	v_lshlrev_b32_e32 v2, 2, v0
	v_mul_lo_u32 v3, v4, s4
	v_readlane_b32 s4, v247, 13
	v_cvt_f32_u32_e32 v9, s1
	v_lshlrev_b32_e32 v6, 2, v13
	v_add3_u32 v5, s4, v2, v3
	v_lshlrev_b32_e32 v2, 3, v12
	v_and_b32_e32 v2, 56, v2
	v_mul_u32_u24_e32 v3, 0x104, v2
	v_add3_u32 v6, s4, v3, v6
	v_rcp_iflag_f32_e32 v3, v9
	s_sub_i32 s4, 0, s1
	v_mov_b32_e32 v1, 0
	v_add_u32_e32 v7, 8, v13
	v_mul_f32_e32 v3, 0x4f7ffffe, v3
	v_cvt_u32_f32_e32 v3, v3
	v_add_u32_e32 v8, 16, v13
	v_add_u32_e32 v9, 24, v13
	v_add_u32_e32 v10, 32, v13
	v_readfirstlane_b32 s10, v3
	s_mul_i32 s4, s4, s10
	s_mul_hi_u32 s4, s10, s4
	s_add_i32 s16, s10, s4
	s_lshl_b32 s4, s0, 1
	s_add_i32 s4, s33, s4
	v_readlane_b32 s10, v247, 8
	s_add_i32 s4, s4, s10
	v_add_u32_e32 v11, 40, v13
	v_add_u32_e32 v14, 48, v13
	v_add_u32_e32 v15, 56, v13
	s_sub_i32 s17, 0xd6ff, s4
	s_movk_i32 s18, 0x4000
	s_mov_b32 s19, 0x8000
	s_mov_b32 s20, 0xc000
	s_mov_b32 s21, 0x10000
	s_mov_b32 s22, 0x14000
	s_mov_b32 s23, 0x18000
	s_mov_b32 s24, 0x1c000
	s_mov_b32 s25, 0x20000
	s_mov_b32 s26, 0x24000
	s_mov_b32 s27, 0x28000
	s_mov_b32 s28, 0x2c000
	s_mov_b32 s29, 0x30000
	s_mov_b32 s30, 0x34000
	s_mov_b32 s31, 0x38000
	s_mov_b32 s34, 0x3c000
	s_mov_b32 s35, 0x40000
	s_mov_b32 s38, 0x44000
	s_mov_b32 s39, 0x48000
	s_mov_b32 s40, 0x4c000
	s_mov_b32 s41, 0x50000
	s_mov_b32 s42, 0x54000
	s_mov_b32 s43, 0x58000
	s_mov_b32 s44, 0x5c000
	s_mov_b32 s45, 0x60000
	s_mov_b32 s46, 0x64000
	s_mov_b32 s47, 0x68000
	s_mov_b32 s48, 0x6c000
	s_mov_b32 s49, 0x70000
	s_mov_b32 s50, 0x74000
	s_mov_b32 s51, 0x78000
	s_mov_b32 s52, 0x7c000
	v_add_u32_e32 v16, 0x410, v5
	v_add_u32_e32 v17, 0x618, v5
	v_add_u32_e32 v18, 0x820, v5
	v_add_u32_e32 v19, 0xa28, v5
	v_add_u32_e32 v20, 0xc30, v5
	v_add_u32_e32 v21, 0xe38, v5
	v_add_u32_e32 v22, 0x1040, v5
	v_add_u32_e32 v23, 0x1248, v5
	v_add_u32_e32 v24, 0x1450, v5
	v_add_u32_e32 v25, 0x1658, v5
	v_add_u32_e32 v26, 0x1860, v5
	v_add_u32_e32 v27, 0x1a68, v5
	v_add_u32_e32 v28, 0x1c70, v5
	v_add_u32_e32 v29, 0x1e78, v5
	v_add_u32_e32 v30, 0x2080, v5
	v_add_u32_e32 v31, 0x2288, v5
	v_add_u32_e32 v32, 0x2490, v5
	v_add_u32_e32 v33, 0x2698, v5
	v_add_u32_e32 v34, 0x28a0, v5
	v_add_u32_e32 v35, 0x2aa8, v5
	v_add_u32_e32 v36, 0x2cb0, v5
	v_add_u32_e32 v37, 0x2eb8, v5
	v_add_u32_e32 v38, 0x30c0, v5
	v_add_u32_e32 v39, 0x32c8, v5
	v_add_u32_e32 v40, 0x34d0, v5
	v_add_u32_e32 v41, 0x36d8, v5
	v_add_u32_e32 v42, 0x38e0, v5
	v_add_u32_e32 v43, 0x3ae8, v5
	v_add_u32_e32 v44, 0x3cf0, v5
	v_add_u32_e32 v45, 0x3ef8, v5
	s_mov_b32 s53, 0xe000
	s_movk_i32 s54, 0xb8
	s_movk_i32 s55, 0x2000
	s_mov_b32 s57, 0xa000
	s_mov_b32 s59, 0x12000
	s_mov_b32 s60, 0x16000
	s_mov_b32 s61, 0x1a000
	s_mov_b32 s62, 0x1e000
	s_mov_b32 s63, 0x22000
	s_mov_b32 s64, 0x26000
	s_mov_b32 s65, 0x2a000
	s_mov_b32 s66, 0x2e000
	s_mov_b32 s67, 0x32000
	s_mov_b32 s68, 0x36000
	s_mov_b32 s69, 0x3a000
	s_mov_b32 s70, 0x3e000
	s_mov_b32 s71, 0xb850
	v_lshlrev_b32_e32 v0, 2, v0
	v_lshlrev_b32_e32 v2, 1, v2
	v_add_u32_e32 v46, 0x400, v6
	s_mov_b32 s72, s56
	s_branch .LBB0_19

.LBB0_828:
	s_add_i32 s15, s0, 0xc00
	s_ashr_i32 s14, s15, 31
	s_lshr_b32 s14, s14, 23
	s_add_i32 s16, s15, s14
	s_ashr_i32 s14, s16, 9
	s_and_b32 s16, s16, 0xfe00
	s_sub_i32 s44, s15, s16
	s_ashr_i32 s15, s14, 31
	s_sext_i32_i16 s45, s44
	s_lshl_b64 s[16:17], s[14:15], 23
	s_bfe_u32 s14, s45, 0x5001a
	s_add_i32 s14, s44, s14
	s_sext_i32_i16 s15, s14
	s_and_b32 s14, s14, 0xffe0
	s_ashr_i32 s46, s15, 5
	s_sub_i32 s14, s44, s14
	s_waitcnt lgkmcnt(0)
	s_add_u32 s47, s10, s16
	s_addc_u32 s15, s11, s17
	s_add_u32 s45, s12, s16
	s_addc_u32 s44, s13, s17
	s_lshl_b32 s16, s46, 6
	s_lshl_b32 s17, s46, 7
	s_sext_i32_i16 s14, s14
	s_and_b32 s46, s17, 0xffffff00
	s_and_b32 s48, s16, 64
	s_ashr_i32 s17, s16, 31
	s_lshl_b32 s14, s14, 6
	s_or_b32 s46, s48, s46
	s_lshl_b64 s[16:17], s[16:17], 2
	v_add_u32_e32 v4, s14, v6
	s_add_u32 s16, s47, s16
	v_ashrrev_i32_e32 v5, 31, v4
	s_addc_u32 s17, s15, s17
	v_lshlrev_b64 v[4:5], 12, v[4:5]
	v_lshl_add_u64 v[58:59], s[16:17], 0, v[0:1]
	v_lshl_add_u64 v[4:5], v[58:59], 0, v[4:5]
	v_add_co_u32_e32 v58, vcc, s1, v4
	s_ashr_i32 s15, s14, 31
	s_nop 0
	v_addc_co_u32_e32 v59, vcc, 0, v5, vcc
	v_add_co_u32_e32 v60, vcc, s4, v4
	v_add_u32_e32 v42, s46, v7
	s_nop 0
	v_addc_co_u32_e32 v61, vcc, 0, v5, vcc
	v_add_co_u32_e32 v62, vcc, s5, v4
	s_lshl_b64 s[14:15], s[14:15], 1
	s_nop 0
	v_addc_co_u32_e32 v63, vcc, 0, v5, vcc
	v_add_co_u32_e32 v64, vcc, s6, v4
	v_add_u32_e32 v44, 8, v42
	s_nop 0
	v_addc_co_u32_e32 v65, vcc, 0, v5, vcc
	v_add_co_u32_e32 v66, vcc, s7, v4
	v_add_u32_e32 v46, 16, v42
	s_nop 0
	v_addc_co_u32_e32 v67, vcc, 0, v5, vcc
	v_add_co_u32_e32 v68, vcc, s8, v4
	v_add_u32_e32 v48, 24, v42
	s_nop 0
	v_addc_co_u32_e32 v69, vcc, 0, v5, vcc
	v_add_co_u32_e32 v70, vcc, s9, v4
	v_add_u32_e32 v50, 32, v42
	s_nop 0
	v_addc_co_u32_e32 v71, vcc, 0, v5, vcc
	v_add_co_u32_e32 v72, vcc, s18, v4
	v_add_u32_e32 v52, 40, v42
	s_nop 0
	v_addc_co_u32_e32 v73, vcc, 0, v5, vcc
	v_add_co_u32_e32 v74, vcc, s19, v4
	v_add_u32_e32 v54, 48, v42
	s_nop 0
	v_addc_co_u32_e32 v75, vcc, 0, v5, vcc
	v_add_co_u32_e32 v76, vcc, s20, v4
	v_add_u32_e32 v56, 56, v42
	s_nop 0
	v_addc_co_u32_e32 v77, vcc, 0, v5, vcc
	v_add_co_u32_e32 v78, vcc, s21, v4
	s_add_u32 s14, s45, s14
	s_nop 0
	v_addc_co_u32_e32 v79, vcc, 0, v5, vcc
	v_add_co_u32_e32 v80, vcc, s22, v4
	v_ashrrev_i32_e32 v43, 31, v42
	s_nop 0
	v_addc_co_u32_e32 v81, vcc, 0, v5, vcc
	v_add_co_u32_e32 v82, vcc, s23, v4
	v_ashrrev_i32_e32 v45, 31, v44
	s_nop 0
	v_addc_co_u32_e32 v83, vcc, 0, v5, vcc
	v_add_co_u32_e32 v84, vcc, s24, v4
	v_ashrrev_i32_e32 v47, 31, v46
	s_nop 0
	v_addc_co_u32_e32 v85, vcc, 0, v5, vcc
	v_add_co_u32_e32 v86, vcc, s25, v4
	v_ashrrev_i32_e32 v49, 31, v48
	s_nop 0
	v_addc_co_u32_e32 v87, vcc, 0, v5, vcc
	v_add_co_u32_e32 v88, vcc, s26, v4
	v_ashrrev_i32_e32 v51, 31, v50
	s_nop 0
	v_addc_co_u32_e32 v89, vcc, 0, v5, vcc
	v_add_co_u32_e32 v90, vcc, s27, v4
	v_ashrrev_i32_e32 v53, 31, v52
	s_nop 0
	v_addc_co_u32_e32 v91, vcc, 0, v5, vcc
	v_add_co_u32_e32 v92, vcc, s28, v4
	v_ashrrev_i32_e32 v55, 31, v54
	s_nop 0
	v_addc_co_u32_e32 v93, vcc, 0, v5, vcc
	v_add_co_u32_e32 v94, vcc, s29, v4
	v_ashrrev_i32_e32 v57, 31, v56
	s_nop 0
	v_addc_co_u32_e32 v95, vcc, 0, v5, vcc
	v_add_co_u32_e32 v96, vcc, s30, v4
	s_addc_u32 s15, s44, s15
	s_nop 0
	v_addc_co_u32_e32 v97, vcc, 0, v5, vcc
	v_add_co_u32_e32 v98, vcc, s31, v4
	v_lshlrev_b64 v[42:43], 12, v[42:43]
	s_nop 0
	v_addc_co_u32_e32 v99, vcc, 0, v5, vcc
	v_add_co_u32_e32 v100, vcc, s34, v4
	v_lshlrev_b64 v[44:45], 12, v[44:45]
	s_nop 0
	v_addc_co_u32_e32 v101, vcc, 0, v5, vcc
	v_add_co_u32_e32 v102, vcc, s35, v4
	v_lshlrev_b64 v[46:47], 12, v[46:47]
	s_nop 0
	v_addc_co_u32_e32 v103, vcc, 0, v5, vcc
	v_add_co_u32_e32 v104, vcc, s36, v4
	v_lshlrev_b64 v[48:49], 12, v[48:49]
	s_nop 0
	v_addc_co_u32_e32 v105, vcc, 0, v5, vcc
	v_add_co_u32_e32 v106, vcc, s37, v4
	v_lshlrev_b64 v[50:51], 12, v[50:51]
	s_nop 0
	v_addc_co_u32_e32 v107, vcc, 0, v5, vcc
	v_add_co_u32_e32 v108, vcc, s38, v4
	v_lshlrev_b64 v[52:53], 12, v[52:53]
	s_nop 0
	v_addc_co_u32_e32 v109, vcc, 0, v5, vcc
	v_add_co_u32_e32 v110, vcc, s39, v4
	v_lshlrev_b64 v[54:55], 12, v[54:55]
	s_nop 0
	v_addc_co_u32_e32 v111, vcc, 0, v5, vcc
	v_add_co_u32_e32 v112, vcc, s40, v4
	v_lshlrev_b64 v[56:57], 12, v[56:57]
	s_nop 0
	v_addc_co_u32_e32 v113, vcc, 0, v5, vcc
	v_add_co_u32_e32 v114, vcc, s41, v4
	v_lshl_add_u64 v[120:121], s[14:15], 0, v[2:3]
	s_nop 0
	v_addc_co_u32_e32 v115, vcc, 0, v5, vcc
	v_add_co_u32_e32 v116, vcc, s42, v4
	v_lshl_add_u64 v[122:123], v[120:121], 0, v[42:43]
	s_nop 0
	v_addc_co_u32_e32 v117, vcc, 0, v5, vcc
	v_add_co_u32_e32 v118, vcc, s43, v4
	v_lshl_add_u64 v[124:125], v[120:121], 0, v[44:45]
	s_nop 0
	v_addc_co_u32_e32 v119, vcc, 0, v5, vcc
	global_load_dwordx2 v[4:5], v[4:5], off nt
	s_nop 0
	global_load_dwordx2 v[58:59], v[58:59], off nt
	s_nop 0
	global_load_dwordx2 v[60:61], v[60:61], off nt
	s_nop 0
	global_load_dwordx2 v[62:63], v[62:63], off nt
	s_nop 0
	global_load_dwordx2 v[64:65], v[64:65], off nt
	s_nop 0
	global_load_dwordx2 v[66:67], v[66:67], off nt
	s_nop 0
	global_load_dwordx2 v[68:69], v[68:69], off nt
	s_nop 0
	global_load_dwordx2 v[70:71], v[70:71], off nt
	s_nop 0
	global_load_dwordx2 v[72:73], v[72:73], off nt
	s_nop 0
	global_load_dwordx2 v[74:75], v[74:75], off nt
	s_nop 0
	global_load_dwordx2 v[76:77], v[76:77], off nt
	s_nop 0
	global_load_dwordx2 v[78:79], v[78:79], off nt
	s_nop 0
	global_load_dwordx2 v[80:81], v[80:81], off nt
	s_nop 0
	global_load_dwordx2 v[82:83], v[82:83], off nt
	s_nop 0
	global_load_dwordx2 v[84:85], v[84:85], off nt
	s_nop 0
	global_load_dwordx2 v[86:87], v[86:87], off nt
	s_nop 0
	global_load_dwordx2 v[88:89], v[88:89], off nt
	s_nop 0
	global_load_dwordx2 v[90:91], v[90:91], off nt
	s_nop 0
	global_load_dwordx2 v[92:93], v[92:93], off nt
	s_nop 0
	global_load_dwordx2 v[94:95], v[94:95], off nt
	s_nop 0
	global_load_dwordx2 v[96:97], v[96:97], off nt
	s_nop 0
	global_load_dwordx2 v[98:99], v[98:99], off nt
	s_nop 0
	global_load_dwordx2 v[100:101], v[100:101], off nt
	s_nop 0
	global_load_dwordx2 v[102:103], v[102:103], off nt
	s_nop 0
	global_load_dwordx2 v[104:105], v[104:105], off nt
	s_nop 0
	global_load_dwordx2 v[106:107], v[106:107], off nt
	s_nop 0
	global_load_dwordx2 v[108:109], v[108:109], off nt
	s_nop 0
	global_load_dwordx2 v[110:111], v[110:111], off nt
	s_nop 0
	global_load_dwordx2 v[112:113], v[112:113], off nt
	s_nop 0
	global_load_dwordx2 v[114:115], v[114:115], off nt
	s_nop 0
	global_load_dwordx2 v[116:117], v[116:117], off nt
	s_nop 0
	global_load_dwordx2 v[118:119], v[118:119], off nt
	s_waitcnt vmcnt(0)
	ds_write2_b32 v9, v4, v5 offset1:1
	ds_write2_b32 v9, v58, v59 offset0:130 offset1:131
	ds_write2_b32 v10, v60, v61 offset1:1
	ds_write2_b32 v11, v62, v63 offset1:1
	ds_write2_b32 v12, v64, v65 offset1:1
	ds_write2_b32 v13, v66, v67 offset1:1
	ds_write2_b32 v14, v68, v69 offset1:1
	ds_write2_b32 v15, v70, v71 offset1:1
	ds_write2_b32 v16, v72, v73 offset1:1
	ds_write2_b32 v17, v74, v75 offset1:1
	ds_write2_b32 v18, v76, v77 offset1:1
	ds_write2_b32 v19, v78, v79 offset1:1
	ds_write2_b32 v20, v80, v81 offset1:1
	ds_write2_b32 v21, v82, v83 offset1:1
	ds_write2_b32 v22, v84, v85 offset1:1
	ds_write2_b32 v23, v86, v87 offset1:1
	ds_write2_b32 v24, v88, v89 offset1:1
	ds_write2_b32 v25, v90, v91 offset1:1
	ds_write2_b32 v26, v92, v93 offset1:1
	ds_write2_b32 v27, v94, v95 offset1:1
	ds_write2_b32 v28, v96, v97 offset1:1
	ds_write2_b32 v29, v98, v99 offset1:1
	ds_write2_b32 v30, v100, v101 offset1:1
	ds_write2_b32 v31, v102, v103 offset1:1
	ds_write2_b32 v32, v104, v105 offset1:1
	ds_write2_b32 v33, v106, v107 offset1:1
	ds_write2_b32 v34, v108, v109 offset1:1
	ds_write2_b32 v35, v110, v111 offset1:1
	ds_write2_b32 v36, v112, v113 offset1:1
	ds_write2_b32 v37, v114, v115 offset1:1
	ds_write2_b32 v38, v116, v117 offset1:1
	ds_write2_b32 v39, v118, v119 offset1:1
	s_waitcnt lgkmcnt(0)
	v_lshl_add_u64 v[126:127], v[120:121], 0, v[46:47]
	v_lshl_add_u64 v[128:129], v[120:121], 0, v[48:49]
	v_lshl_add_u64 v[130:131], v[120:121], 0, v[50:51]
	v_lshl_add_u64 v[132:133], v[120:121], 0, v[52:53]
	v_lshl_add_u64 v[134:135], v[120:121], 0, v[54:55]
	v_lshl_add_u64 v[120:121], v[120:121], 0, v[56:57]
	ds_read2_b32 v[4:5], v8 offset0:65 offset1:73
	ds_read2_b32 v[46:47], v8 offset1:8
	ds_read2_b32 v[48:49], v8 offset0:130 offset1:138
	ds_read2_b32 v[50:51], v8 offset0:195 offset1:203
	ds_read2_b32 v[52:53], v40 offset0:4 offset1:12
	ds_read2_b32 v[54:55], v40 offset0:69 offset1:77
	ds_read2_b32 v[56:57], v40 offset0:134 offset1:142
	ds_read2_b32 v[58:59], v40 offset0:199 offset1:207
	ds_read2_b32 v[60:61], v8 offset0:81 offset1:89
	ds_read2_b32 v[62:63], v8 offset0:16 offset1:24
	ds_read2_b32 v[64:65], v8 offset0:146 offset1:154
	ds_read2_b32 v[66:67], v8 offset0:211 offset1:219
	ds_read2_b32 v[68:69], v40 offset0:20 offset1:28
	ds_read2_b32 v[70:71], v40 offset0:85 offset1:93
	ds_read2_b32 v[72:73], v40 offset0:150 offset1:158
	ds_read2_b32 v[74:75], v40 offset0:215 offset1:223
	ds_read2_b32 v[76:77], v8 offset0:32 offset1:40
	ds_read2_b32 v[78:79], v8 offset0:97 offset1:105
	ds_read2_b32 v[80:81], v8 offset0:162 offset1:170
	ds_read2_b32 v[82:83], v8 offset0:227 offset1:235
	ds_read2_b32 v[84:85], v40 offset0:36 offset1:44
	ds_read2_b32 v[86:87], v40 offset0:101 offset1:109
	ds_read2_b32 v[88:89], v40 offset0:166 offset1:174
	ds_read2_b32 v[90:91], v40 offset0:231 offset1:239
	ds_read2_b32 v[92:93], v8 offset0:48 offset1:56
	ds_read2_b32 v[94:95], v8 offset0:113 offset1:121
	ds_read2_b32 v[96:97], v8 offset0:178 offset1:186
	ds_read2_b32 v[98:99], v8 offset0:243 offset1:251
	ds_read2_b32 v[100:101], v40 offset0:52 offset1:60
	ds_read2_b32 v[102:103], v40 offset0:117 offset1:125
	ds_read2_b32 v[104:105], v40 offset0:182 offset1:190
	ds_read2_b32 v[106:107], v40 offset0:247 offset1:255
	s_waitcnt lgkmcnt(14)
	v_cvt_pk_bf16_f32 v42, v46, v4
	v_cvt_pk_bf16_f32 v43, v48, v50
	v_cvt_pk_bf16_f32 v44, v52, v54
	v_cvt_pk_bf16_f32 v45, v56, v58
	v_cvt_pk_bf16_f32 v46, v47, v5
	v_cvt_pk_bf16_f32 v47, v49, v51
	v_cvt_pk_bf16_f32 v48, v53, v55
	v_cvt_pk_bf16_f32 v49, v57, v59
	v_cvt_pk_bf16_f32 v50, v62, v60
	v_cvt_pk_bf16_f32 v51, v64, v66
	v_cvt_pk_bf16_f32 v52, v68, v70
	v_cvt_pk_bf16_f32 v53, v72, v74
	v_cvt_pk_bf16_f32 v54, v63, v61
	v_cvt_pk_bf16_f32 v55, v65, v67
	v_cvt_pk_bf16_f32 v56, v69, v71
	v_cvt_pk_bf16_f32 v57, v73, v75
	v_cvt_pk_bf16_f32 v58, v76, v78
	s_waitcnt lgkmcnt(12)
	v_cvt_pk_bf16_f32 v59, v80, v82
	s_waitcnt lgkmcnt(10)
	v_cvt_pk_bf16_f32 v60, v84, v86
	s_waitcnt lgkmcnt(8)
	v_cvt_pk_bf16_f32 v61, v88, v90
	v_cvt_pk_bf16_f32 v62, v77, v79
	v_cvt_pk_bf16_f32 v63, v81, v83
	v_cvt_pk_bf16_f32 v64, v85, v87
	v_cvt_pk_bf16_f32 v65, v89, v91
	s_waitcnt lgkmcnt(6)
	v_cvt_pk_bf16_f32 v66, v92, v94
	s_waitcnt lgkmcnt(4)
	v_cvt_pk_bf16_f32 v67, v96, v98
	s_waitcnt lgkmcnt(2)
	v_cvt_pk_bf16_f32 v68, v100, v102
	s_waitcnt lgkmcnt(0)
	v_cvt_pk_bf16_f32 v69, v104, v106
	v_cvt_pk_bf16_f32 v70, v93, v95
	v_cvt_pk_bf16_f32 v71, v97, v99
	v_cvt_pk_bf16_f32 v72, v101, v103
	v_cvt_pk_bf16_f32 v73, v105, v107
	global_store_dwordx4 v[122:123], v[42:45], off nt
	global_store_dwordx4 v[124:125], v[46:49], off nt
	global_store_dwordx4 v[126:127], v[50:53], off nt
	global_store_dwordx4 v[128:129], v[54:57], off nt
	global_store_dwordx4 v[130:131], v[58:61], off nt
	global_store_dwordx4 v[132:133], v[62:65], off nt
	global_store_dwordx4 v[134:135], v[66:69], off nt
	global_store_dwordx4 v[120:121], v[70:73], off nt
	s_waitcnt lgkmcnt(0)
	s_addk_i32 s0, 0x400
	s_cmpk_gt_i32 s0, 0xbff
	s_cbranch_scc0 .LBB0_828

.LBB0_2219:
	s_add_i32 s11, s0, 0xc00
	s_ashr_i32 s10, s11, 31
	s_lshr_b32 s10, s10, 23
	s_add_i32 s12, s11, s10
	s_ashr_i32 s10, s12, 9
	s_and_b32 s12, s12, 0xfe00
	s_sub_i32 s12, s11, s12
	s_sext_i32_i16 s13, s12
	s_bfe_u32 s13, s13, 0x5001a
	s_add_i32 s13, s12, s13
	s_ashr_i32 s11, s10, 31
	s_sext_i32_i16 s44, s13
	s_and_b32 s13, s13, 0xffe0
	s_lshl_b64 s[10:11], s[10:11], 23
	s_ashr_i32 s46, s44, 5
	s_sub_i32 s12, s12, s13
	s_add_u32 s10, s10, 0x8000000
	s_sext_i32_i16 s13, s12
	s_addc_u32 s12, s11, 0
	s_waitcnt lgkmcnt(0)
	s_add_u32 s47, s6, s10
	s_addc_u32 s11, s7, s12
	s_add_u32 s45, s8, s10
	s_addc_u32 s44, s9, s12
	s_lshl_b32 s12, s46, 6
	s_lshl_b32 s10, s13, 6
	s_lshl_b32 s13, s46, 7
	s_and_b32 s46, s13, 0xffffff00
	s_and_b32 s48, s12, 64
	s_ashr_i32 s13, s12, 31
	s_or_b32 s46, s48, s46
	s_lshl_b64 s[12:13], s[12:13], 2
	v_add_u32_e32 v4, s10, v74
	s_add_u32 s12, s47, s12
	v_ashrrev_i32_e32 v5, 31, v4
	s_addc_u32 s13, s11, s13
	v_lshlrev_b64 v[4:5], 12, v[4:5]
	v_lshl_add_u64 v[56:57], s[12:13], 0, v[0:1]
	v_lshl_add_u64 v[4:5], v[56:57], 0, v[4:5]
	v_add_co_u32_e32 v56, vcc, s1, v4
	s_ashr_i32 s11, s10, 31
	s_nop 0
	v_addc_co_u32_e32 v57, vcc, 0, v5, vcc
	v_add_co_u32_e32 v58, vcc, s4, v4
	v_add_u32_e32 v40, s46, v75
	s_nop 0
	v_addc_co_u32_e32 v59, vcc, 0, v5, vcc
	v_add_co_u32_e32 v60, vcc, s5, v4
	s_lshl_b64 s[10:11], s[10:11], 1
	s_nop 0
	v_addc_co_u32_e32 v61, vcc, 0, v5, vcc
	v_add_co_u32_e32 v62, vcc, s14, v4
	v_add_u32_e32 v42, 8, v40
	s_nop 0
	v_addc_co_u32_e32 v63, vcc, 0, v5, vcc
	v_add_co_u32_e32 v64, vcc, s15, v4
	v_add_u32_e32 v44, 16, v40
	s_nop 0
	v_addc_co_u32_e32 v65, vcc, 0, v5, vcc
	v_add_co_u32_e32 v66, vcc, s16, v4
	v_add_u32_e32 v46, 24, v40
	s_nop 0
	v_addc_co_u32_e32 v67, vcc, 0, v5, vcc
	v_add_co_u32_e32 v68, vcc, s17, v4
	v_add_u32_e32 v48, 32, v40
	s_nop 0
	v_addc_co_u32_e32 v69, vcc, 0, v5, vcc
	v_add_co_u32_e32 v70, vcc, s18, v4
	v_add_u32_e32 v50, 40, v40
	s_nop 0
	v_addc_co_u32_e32 v71, vcc, 0, v5, vcc
	v_add_co_u32_e32 v72, vcc, s19, v4
	v_add_u32_e32 v52, 48, v40
	s_nop 0
	v_addc_co_u32_e32 v73, vcc, 0, v5, vcc
	v_add_co_u32_e32 v76, vcc, s20, v4
	v_add_u32_e32 v54, 56, v40
	s_nop 0
	v_addc_co_u32_e32 v77, vcc, 0, v5, vcc
	v_add_co_u32_e32 v78, vcc, s21, v4
	s_add_u32 s10, s45, s10
	s_nop 0
	v_addc_co_u32_e32 v79, vcc, 0, v5, vcc
	v_add_co_u32_e32 v80, vcc, s22, v4
	v_ashrrev_i32_e32 v41, 31, v40
	s_nop 0
	v_addc_co_u32_e32 v81, vcc, 0, v5, vcc
	v_add_co_u32_e32 v82, vcc, s23, v4
	v_ashrrev_i32_e32 v43, 31, v42
	s_nop 0
	v_addc_co_u32_e32 v83, vcc, 0, v5, vcc
	v_add_co_u32_e32 v84, vcc, s24, v4
	v_ashrrev_i32_e32 v45, 31, v44
	s_nop 0
	v_addc_co_u32_e32 v85, vcc, 0, v5, vcc
	v_add_co_u32_e32 v86, vcc, s25, v4
	v_ashrrev_i32_e32 v47, 31, v46
	s_nop 0
	v_addc_co_u32_e32 v87, vcc, 0, v5, vcc
	v_add_co_u32_e32 v88, vcc, s26, v4
	v_ashrrev_i32_e32 v49, 31, v48
	s_nop 0
	v_addc_co_u32_e32 v89, vcc, 0, v5, vcc
	v_add_co_u32_e32 v90, vcc, s27, v4
	v_ashrrev_i32_e32 v51, 31, v50
	s_nop 0
	v_addc_co_u32_e32 v91, vcc, 0, v5, vcc
	v_add_co_u32_e32 v92, vcc, s28, v4
	v_ashrrev_i32_e32 v53, 31, v52
	s_nop 0
	v_addc_co_u32_e32 v93, vcc, 0, v5, vcc
	v_add_co_u32_e32 v94, vcc, s29, v4
	v_ashrrev_i32_e32 v55, 31, v54
	s_nop 0
	v_addc_co_u32_e32 v95, vcc, 0, v5, vcc
	v_add_co_u32_e32 v96, vcc, s30, v4
	s_addc_u32 s11, s44, s11
	s_nop 0
	v_addc_co_u32_e32 v97, vcc, 0, v5, vcc
	v_add_co_u32_e32 v98, vcc, s31, v4
	v_lshlrev_b64 v[40:41], 12, v[40:41]
	s_nop 0
	v_addc_co_u32_e32 v99, vcc, 0, v5, vcc
	v_add_co_u32_e32 v100, vcc, s34, v4
	v_lshlrev_b64 v[42:43], 12, v[42:43]
	s_nop 0
	v_addc_co_u32_e32 v101, vcc, 0, v5, vcc
	v_add_co_u32_e32 v102, vcc, s35, v4
	v_lshlrev_b64 v[44:45], 12, v[44:45]
	s_nop 0
	v_addc_co_u32_e32 v103, vcc, 0, v5, vcc
	v_add_co_u32_e32 v104, vcc, s36, v4
	v_lshlrev_b64 v[46:47], 12, v[46:47]
	s_nop 0
	v_addc_co_u32_e32 v105, vcc, 0, v5, vcc
	v_add_co_u32_e32 v106, vcc, s37, v4
	v_lshlrev_b64 v[48:49], 12, v[48:49]
	s_nop 0
	v_addc_co_u32_e32 v107, vcc, 0, v5, vcc
	v_add_co_u32_e32 v108, vcc, s38, v4
	v_lshlrev_b64 v[50:51], 12, v[50:51]
	s_nop 0
	v_addc_co_u32_e32 v109, vcc, 0, v5, vcc
	v_add_co_u32_e32 v110, vcc, s39, v4
	v_lshlrev_b64 v[52:53], 12, v[52:53]
	s_nop 0
	v_addc_co_u32_e32 v111, vcc, 0, v5, vcc
	v_add_co_u32_e32 v112, vcc, s40, v4
	v_lshlrev_b64 v[54:55], 12, v[54:55]
	s_nop 0
	v_addc_co_u32_e32 v113, vcc, 0, v5, vcc
	v_add_co_u32_e32 v114, vcc, s41, v4
	v_lshl_add_u64 v[120:121], s[10:11], 0, v[2:3]
	s_nop 0
	v_addc_co_u32_e32 v115, vcc, 0, v5, vcc
	v_add_co_u32_e32 v116, vcc, s42, v4
	v_lshl_add_u64 v[122:123], v[120:121], 0, v[40:41]
	s_nop 0
	v_addc_co_u32_e32 v117, vcc, 0, v5, vcc
	v_add_co_u32_e32 v118, vcc, s43, v4
	v_lshl_add_u64 v[124:125], v[120:121], 0, v[42:43]
	s_nop 0
	v_addc_co_u32_e32 v119, vcc, 0, v5, vcc
	global_load_dwordx2 v[4:5], v[4:5], off nt
	s_nop 0
	global_load_dwordx2 v[56:57], v[56:57], off nt
	s_nop 0
	global_load_dwordx2 v[58:59], v[58:59], off nt
	s_nop 0
	global_load_dwordx2 v[60:61], v[60:61], off nt
	s_nop 0
	global_load_dwordx2 v[62:63], v[62:63], off nt
	s_nop 0
	global_load_dwordx2 v[64:65], v[64:65], off nt
	s_nop 0
	global_load_dwordx2 v[66:67], v[66:67], off nt
	s_nop 0
	global_load_dwordx2 v[68:69], v[68:69], off nt
	s_nop 0
	global_load_dwordx2 v[70:71], v[70:71], off nt
	s_nop 0
	global_load_dwordx2 v[72:73], v[72:73], off nt
	s_nop 0
	global_load_dwordx2 v[76:77], v[76:77], off nt
	s_nop 0
	global_load_dwordx2 v[78:79], v[78:79], off nt
	s_nop 0
	global_load_dwordx2 v[80:81], v[80:81], off nt
	s_nop 0
	global_load_dwordx2 v[82:83], v[82:83], off nt
	s_nop 0
	global_load_dwordx2 v[84:85], v[84:85], off nt
	s_nop 0
	global_load_dwordx2 v[86:87], v[86:87], off nt
	s_nop 0
	global_load_dwordx2 v[88:89], v[88:89], off nt
	s_nop 0
	global_load_dwordx2 v[90:91], v[90:91], off nt
	s_nop 0
	global_load_dwordx2 v[92:93], v[92:93], off nt
	s_nop 0
	global_load_dwordx2 v[94:95], v[94:95], off nt
	s_nop 0
	global_load_dwordx2 v[96:97], v[96:97], off nt
	s_nop 0
	global_load_dwordx2 v[98:99], v[98:99], off nt
	s_nop 0
	global_load_dwordx2 v[100:101], v[100:101], off nt
	s_nop 0
	global_load_dwordx2 v[102:103], v[102:103], off nt
	s_nop 0
	global_load_dwordx2 v[104:105], v[104:105], off nt
	s_nop 0
	global_load_dwordx2 v[106:107], v[106:107], off nt
	s_nop 0
	global_load_dwordx2 v[108:109], v[108:109], off nt
	s_nop 0
	global_load_dwordx2 v[110:111], v[110:111], off nt
	s_nop 0
	global_load_dwordx2 v[112:113], v[112:113], off nt
	s_nop 0
	global_load_dwordx2 v[114:115], v[114:115], off nt
	s_nop 0
	global_load_dwordx2 v[116:117], v[116:117], off nt
	s_nop 0
	global_load_dwordx2 v[118:119], v[118:119], off nt
	s_waitcnt vmcnt(0)
	ds_write2_b32 v7, v4, v5 offset1:1
	ds_write2_b32 v7, v56, v57 offset0:130 offset1:131
	ds_write2_b32 v8, v58, v59 offset1:1
	ds_write2_b32 v9, v60, v61 offset1:1
	ds_write2_b32 v10, v62, v63 offset1:1
	ds_write2_b32 v11, v64, v65 offset1:1
	ds_write2_b32 v12, v66, v67 offset1:1
	ds_write2_b32 v13, v68, v69 offset1:1
	ds_write2_b32 v14, v70, v71 offset1:1
	ds_write2_b32 v15, v72, v73 offset1:1
	ds_write2_b32 v16, v76, v77 offset1:1
	ds_write2_b32 v17, v78, v79 offset1:1
	ds_write2_b32 v18, v80, v81 offset1:1
	ds_write2_b32 v19, v82, v83 offset1:1
	ds_write2_b32 v20, v84, v85 offset1:1
	ds_write2_b32 v21, v86, v87 offset1:1
	ds_write2_b32 v22, v88, v89 offset1:1
	ds_write2_b32 v23, v90, v91 offset1:1
	ds_write2_b32 v24, v92, v93 offset1:1
	ds_write2_b32 v25, v94, v95 offset1:1
	ds_write2_b32 v26, v96, v97 offset1:1
	ds_write2_b32 v27, v98, v99 offset1:1
	ds_write2_b32 v28, v100, v101 offset1:1
	ds_write2_b32 v29, v102, v103 offset1:1
	ds_write2_b32 v30, v104, v105 offset1:1
	ds_write2_b32 v31, v106, v107 offset1:1
	ds_write2_b32 v32, v108, v109 offset1:1
	ds_write2_b32 v33, v110, v111 offset1:1
	ds_write2_b32 v34, v112, v113 offset1:1
	ds_write2_b32 v35, v114, v115 offset1:1
	ds_write2_b32 v36, v116, v117 offset1:1
	ds_write2_b32 v37, v118, v119 offset1:1
	s_waitcnt lgkmcnt(0)
	v_lshl_add_u64 v[126:127], v[120:121], 0, v[44:45]
	v_lshl_add_u64 v[128:129], v[120:121], 0, v[46:47]
	v_lshl_add_u64 v[130:131], v[120:121], 0, v[48:49]
	v_lshl_add_u64 v[132:133], v[120:121], 0, v[50:51]
	v_lshl_add_u64 v[134:135], v[120:121], 0, v[52:53]
	v_lshl_add_u64 v[120:121], v[120:121], 0, v[54:55]
	ds_read2_b32 v[4:5], v6 offset0:65 offset1:73
	ds_read2_b32 v[44:45], v6 offset1:8
	ds_read2_b32 v[46:47], v6 offset0:130 offset1:138
	ds_read2_b32 v[48:49], v6 offset0:195 offset1:203
	ds_read2_b32 v[50:51], v38 offset0:4 offset1:12
	ds_read2_b32 v[52:53], v38 offset0:69 offset1:77
	ds_read2_b32 v[54:55], v38 offset0:134 offset1:142
	ds_read2_b32 v[56:57], v38 offset0:199 offset1:207
	ds_read2_b32 v[58:59], v6 offset0:81 offset1:89
	ds_read2_b32 v[60:61], v6 offset0:16 offset1:24
	ds_read2_b32 v[62:63], v6 offset0:146 offset1:154
	ds_read2_b32 v[64:65], v6 offset0:211 offset1:219
	ds_read2_b32 v[66:67], v38 offset0:20 offset1:28
	ds_read2_b32 v[68:69], v38 offset0:85 offset1:93
	ds_read2_b32 v[70:71], v38 offset0:150 offset1:158
	ds_read2_b32 v[72:73], v38 offset0:215 offset1:223
	ds_read2_b32 v[76:77], v6 offset0:32 offset1:40
	ds_read2_b32 v[78:79], v6 offset0:97 offset1:105
	ds_read2_b32 v[80:81], v6 offset0:162 offset1:170
	ds_read2_b32 v[82:83], v6 offset0:227 offset1:235
	ds_read2_b32 v[84:85], v38 offset0:36 offset1:44
	ds_read2_b32 v[86:87], v38 offset0:101 offset1:109
	ds_read2_b32 v[88:89], v38 offset0:166 offset1:174
	ds_read2_b32 v[90:91], v38 offset0:231 offset1:239
	ds_read2_b32 v[92:93], v6 offset0:48 offset1:56
	ds_read2_b32 v[94:95], v6 offset0:113 offset1:121
	ds_read2_b32 v[96:97], v6 offset0:178 offset1:186
	ds_read2_b32 v[98:99], v6 offset0:243 offset1:251
	ds_read2_b32 v[100:101], v38 offset0:52 offset1:60
	ds_read2_b32 v[102:103], v38 offset0:117 offset1:125
	ds_read2_b32 v[104:105], v38 offset0:182 offset1:190
	ds_read2_b32 v[106:107], v38 offset0:247 offset1:255
	s_waitcnt lgkmcnt(14)
	v_cvt_pk_bf16_f32 v40, v44, v4
	v_cvt_pk_bf16_f32 v41, v46, v48
	v_cvt_pk_bf16_f32 v42, v50, v52
	v_cvt_pk_bf16_f32 v43, v54, v56
	v_cvt_pk_bf16_f32 v44, v45, v5
	v_cvt_pk_bf16_f32 v45, v47, v49
	v_cvt_pk_bf16_f32 v46, v51, v53
	v_cvt_pk_bf16_f32 v47, v55, v57
	v_cvt_pk_bf16_f32 v48, v60, v58
	v_cvt_pk_bf16_f32 v49, v62, v64
	v_cvt_pk_bf16_f32 v50, v66, v68
	v_cvt_pk_bf16_f32 v51, v70, v72
	v_cvt_pk_bf16_f32 v52, v61, v59
	v_cvt_pk_bf16_f32 v53, v63, v65
	v_cvt_pk_bf16_f32 v54, v67, v69
	v_cvt_pk_bf16_f32 v55, v71, v73
	v_cvt_pk_bf16_f32 v56, v76, v78
	s_waitcnt lgkmcnt(12)
	v_cvt_pk_bf16_f32 v57, v80, v82
	s_waitcnt lgkmcnt(10)
	v_cvt_pk_bf16_f32 v58, v84, v86
	s_waitcnt lgkmcnt(8)
	v_cvt_pk_bf16_f32 v59, v88, v90
	v_cvt_pk_bf16_f32 v60, v77, v79
	v_cvt_pk_bf16_f32 v61, v81, v83
	v_cvt_pk_bf16_f32 v62, v85, v87
	v_cvt_pk_bf16_f32 v63, v89, v91
	s_waitcnt lgkmcnt(6)
	v_cvt_pk_bf16_f32 v64, v92, v94
	s_waitcnt lgkmcnt(4)
	v_cvt_pk_bf16_f32 v65, v96, v98
	s_waitcnt lgkmcnt(2)
	v_cvt_pk_bf16_f32 v66, v100, v102
	s_waitcnt lgkmcnt(0)
	v_cvt_pk_bf16_f32 v67, v104, v106
	v_cvt_pk_bf16_f32 v68, v93, v95
	v_cvt_pk_bf16_f32 v69, v97, v99
	v_cvt_pk_bf16_f32 v70, v101, v103
	v_cvt_pk_bf16_f32 v71, v105, v107
	global_store_dwordx4 v[122:123], v[40:43], off nt
	global_store_dwordx4 v[124:125], v[44:47], off nt
	global_store_dwordx4 v[126:127], v[48:51], off nt
	global_store_dwordx4 v[128:129], v[52:55], off nt
	global_store_dwordx4 v[130:131], v[56:59], off nt
	global_store_dwordx4 v[132:133], v[60:63], off nt
	global_store_dwordx4 v[134:135], v[64:67], off nt
	global_store_dwordx4 v[120:121], v[68:71], off nt
	s_waitcnt lgkmcnt(0)
	s_addk_i32 s0, 0x400
	s_cmpk_gt_i32 s0, 0xbff
	s_cbranch_scc0 .LBB0_2219
